# grid barriers P3->P4 and P4->P5 replaced by XCD-local barriers (no L2 write-back) when every workgroup sits on XCD index%8, checked at start; full barrier otherwise
# speedup vs baseline: 1.0102x; 1.0090x over previous
.LBB0_2:
	v_lshl_add_u32 v1, v0, 2, 0
	v_add_u32_e32 v1, 0x20000, v1
	v_mov_b32_e32 v2, 0
	ds_write2st64_b32 v1, v2, v2 offset1:8
	ds_write2st64_b32 v1, v2, v2 offset0:16 offset1:24
	v_or_b32_e32 v1, 0x800, v0
	s_mov_b64 s[2:3], -1
	s_and_saveexec_b64 s[4:5], s[2:3]
	v_lshl_add_u32 v3, v1, 2, 0
	v_add_u32_e32 v3, 0x20000, v3
	ds_write_b32 v3, v2
	s_or_b64 exec, exec, s[4:5]
	s_load_dwordx8 s[52:59], s[0:1], 0x80
	s_load_dwordx2 s[90:91], s[0:1], 0xa0
	s_load_dwordx4 s[80:83], s[0:1], 0xa8
	s_and_saveexec_b64 s[4:5], s[2:3]
	s_add_i32 s2, 0, 0x20000
	v_lshl_add_u32 v1, v1, 2, s2
	v_mov_b32_e32 v2, 0
	ds_write_b32 v1, v2 offset:2048
	s_or_b64 exec, exec, s[4:5]
	v_or_b32_e32 v1, 0xc00, v0
	v_cmp_gt_u32_e64 s[2:3], 7, 6
	v_cmp_gt_u32_e64 s[6:7], 7, 5
	s_and_saveexec_b64 s[4:5], s[6:7]
	v_lshl_add_u32 v2, v1, 2, 0
	v_add_u32_e32 v2, 0x20000, v2
	v_mov_b32_e32 v3, 0
	ds_write_b32 v2, v3
	s_or_b64 exec, exec, s[4:5]
	s_and_saveexec_b64 s[4:5], s[2:3]
	s_add_i32 s2, 0, 0x20000
	v_lshl_add_u32 v1, v1, 2, s2
	v_mov_b32_e32 v2, 0
	ds_write_b32 v1, v2 offset:2048
	s_or_b64 exec, exec, s[4:5]
	s_load_dwordx16 s[12:27], s[0:1], 0x0
	s_load_dwordx16 s[36:51], s[0:1], 0x40
	s_waitcnt lgkmcnt(0)
	s_mul_i32 s0, s82, 0xd80
	s_ashr_i32 s1, s0, 31
	s_lshl_b64 s[0:1], s[0:1], 2
	s_add_u32 s0, s90, s0
	s_addc_u32 s1, s91, s1
	s_add_u32 s0, s0, 0x4000
	s_addc_u32 s1, s1, 0
	v_writelane_b32 v255, s0, 9
	s_barrier
	s_nop 0
	v_writelane_b32 v255, s1, 10
	s_getreg_b32 s0, hwreg(HW_REG_XCC_ID, 0, 4)
	s_and_b32 s0, s0, 15
	v_writelane_b32 v255, s0, 11
	v_cmp_eq_u32_e64 s[2:3], 0, v0
	s_mov_b64 s[0:1], exec
	s_nop 0
	v_writelane_b32 v255, s2, 12
	s_nop 1
	v_writelane_b32 v255, s3, 13
	s_and_b64 s[2:3], s[0:1], s[2:3]
	s_mov_b64 exec, s[2:3]
	s_cbranch_execz .LBB0_13
	s_mov_b64 s[2:3], exec
	v_mbcnt_lo_u32_b32 v1, s2, 0
	v_mbcnt_hi_u32_b32 v1, s3, v1
	v_cmp_eq_u32_e32 vcc, 0, v1
	s_and_b64 s[4:5], exec, vcc
	s_mov_b64 exec, s[4:5]
	s_cbranch_execz .LBB0_13
	v_readlane_b32 s4, v255, 11
	s_bcnt1_i32_b64 s2, s[2:3]
	s_lshl_b32 s4, s4, 8
	v_mov_b32_e32 v2, s2
	v_readlane_b32 s2, v255, 9
	v_mov_b32_e32 v1, s4
	v_readlane_b32 s3, v255, 10
	s_nop 4
	global_atomic_add v1, v2, s[2:3] offset:1024
	v_readlane_b32 s4, v255, 7
	v_readlane_b32 s5, v255, 11
	s_and_b32 s4, s4, 7
	s_sub_u32 s4, s4, s5
	v_readlane_b32 s5, v255, 2
	s_xor_b32 s5, s5, 0x100
	s_or_b32 s4, s4, s5
	s_cmp_eq_u32 s4, 0
	s_cbranch_scc1 .Lplace_ok
	v_mov_b32_e32 v1, 0x3000
	v_mov_b32_e32 v2, 1
	global_atomic_add v1, v2, s[2:3] offset:896
.Lplace_ok:
.LBB0_13:
	s_or_b64 exec, exec, s[0:1]
	s_add_u32 s72, s90, 0x100000
	s_addc_u32 s73, s91, 0
	s_add_u32 s70, s90, 0xe00000
	s_addc_u32 s71, s91, 0
	s_add_u32 s0, s90, 0xd800000
	s_addc_u32 s1, s91, 0
	s_add_u32 s74, s90, 0x200000
	v_writelane_b32 v255, s0, 14
	s_addc_u32 s75, s91, 0
	s_nop 0
	v_writelane_b32 v255, s1, 15
	s_add_u32 s0, s90, 0x1100000
	s_addc_u32 s1, s91, 0
	v_writelane_b32 v255, s0, 16
	s_nop 1
	v_writelane_b32 v255, s1, 17
	s_lshr_b32 s0, s10, 6
	v_readlane_b32 s5, v255, 2
	s_abs_i32 s94, s5
	v_cvt_f32_u32_e32 v1, s94
	s_sub_i32 s2, 0, s94
	v_writelane_b32 v255, s0, 18
	s_add_i32 s0, s5, 0xfff
	v_rcp_iflag_f32_e32 v1, v1
	s_ashr_i32 s1, s0, 31
	s_abs_i32 s0, s0
	s_ashr_i32 s6, s5, 31
	v_mul_f32_e32 v1, 0x4f7ffffe, v1
	v_cvt_u32_f32_e32 v1, v1
	s_xor_b32 s1, s1, s6
	v_writelane_b32 v255, s6, 19
	v_readfirstlane_b32 s3, v1
	s_mul_i32 s2, s2, s3
	s_mul_hi_u32 s2, s3, s2
	s_add_i32 s96, s3, s2
	s_mul_hi_u32 s2, s0, s96
	s_mul_i32 s3, s2, s94
	s_sub_i32 s0, s0, s3
	s_add_i32 s4, s2, 1
	s_sub_i32 s3, s0, s94
	s_cmp_ge_u32 s0, s94
	s_cselect_b32 s2, s4, s2
	s_cselect_b32 s0, s3, s0
	s_add_i32 s3, s2, 1
	s_cmp_ge_u32 s0, s94
	s_cselect_b32 s0, s3, s2
	s_xor_b32 s0, s0, s1
	s_sub_i32 s33, s0, s1
	s_add_i32 s0, s5, 0xbfff
	s_ashr_i32 s1, s0, 31
	s_abs_i32 s0, s0
	s_mul_hi_u32 s2, s0, s96
	s_mul_i32 s3, s2, s94
	s_sub_i32 s0, s0, s3
	s_xor_b32 s1, s1, s6
	s_add_i32 s3, s2, 1
	s_sub_i32 s4, s0, s94
	s_cmp_ge_u32 s0, s94
	s_cselect_b32 s2, s3, s2
	s_cselect_b32 s0, s4, s0
	s_add_i32 s3, s2, 1
	s_cmp_ge_u32 s0, s94
	s_cselect_b32 s0, s3, s2
	s_xor_b32 s0, s0, s1
	s_sub_i32 s0, s0, s1
	s_min_i32 s34, s0, 0
	s_add_i32 s34, s34, s33
	s_cmp_lt_i32 s80, 1
	v_writelane_b32 v255, s0, 20
	s_cselect_b64 s[0:1], -1, 0
	s_cmp_gt_i32 s81, 0
	s_cselect_b64 s[2:3], -1, 0
	v_writelane_b32 v255, s90, 21
	s_and_b64 s[68:69], s[0:1], s[2:3]
	s_mov_b64 s[0:1], s[80:81]
	v_writelane_b32 v255, s91, 22
	v_writelane_b32 v255, s0, 23
	s_andn2_b64 vcc, exec, s[68:69]
	v_and_b32_e32 v1, 63, v0
	v_writelane_b32 v255, s1, 24
	v_writelane_b32 v255, s2, 25
	v_writelane_b32 v255, s3, 26
	v_writelane_b32 v255, s10, 27
	s_cbranch_vccnz .LBB0_220
	v_readlane_b32 s0, v255, 2
	s_lshl_b32 s4, s0, 2
	s_abs_i32 s2, s4
	v_cvt_f32_u32_e32 v2, s2
	s_movk_i32 s0, 0x1010
	s_add_i32 s5, s4, 0x3fff
	s_abs_i32 s3, s5
	v_rcp_iflag_f32_e32 v3, v2
	v_lshl_or_b32 v2, s93, 9, v0
	v_cmp_gt_i32_e32 vcc, s0, v2
	s_sub_i32 s0, 0, s2
	v_mul_f32_e32 v3, 0x4f7ffffe, v3
	v_cvt_u32_f32_e32 v3, v3
	s_nop 0
	v_readfirstlane_b32 s6, v3
	s_mul_i32 s0, s0, s6
	s_mul_hi_u32 s0, s6, s0
	s_add_i32 s6, s6, s0
	s_and_saveexec_b64 s[0:1], vcc
	s_cbranch_execz .LBB0_16
	s_mov_b32 s7, 0x7f807f81
	v_mul_hi_i32 v3, v2, s7
	v_lshrrev_b32_e32 v4, 31, v3
	v_ashrrev_i32_e32 v3, 7, v3
	v_add_u32_e32 v3, v3, v4
	v_mul_i32_i24_e32 v4, 0x101, v3
	v_sub_u32_e32 v4, v2, v4
	v_ashrrev_i32_e32 v5, 31, v4
	s_getpc_b64 s[8:9]
	s_add_u32 s8, s8, _ZL5BKT_A@rel32@lo+4
	s_addc_u32 s9, s9, _ZL5BKT_A@rel32@hi+12
	v_lshl_add_u64 v[6:7], s[8:9], 0, v[4:5]
	global_load_ubyte v6, v[6:7], off
	s_movk_i32 s7, 0x404
	s_waitcnt vmcnt(0)
	v_mad_u32_u24 v6, v6, 28, v3
	v_ashrrev_i32_e32 v7, 31, v6
	v_lshl_add_u64 v[6:7], v[6:7], 2, s[22:23]
	global_load_dword v8, v[6:7], off
	v_mov_b64_e32 v[6:7], s[72:73]
	v_mad_i64_i32 v[6:7], s[8:9], v3, s7, v[6:7]
	v_lshl_add_u64 v[4:5], v[4:5], 2, v[6:7]
	s_waitcnt vmcnt(0)
	global_store_dword v[4:5], v8, off

.LBB0_899:
	s_cmp_gt_i32 s81, 4
	s_cselect_b64 s[0:1], -1, 0
	s_and_b64 s[4:5], s[16:17], s[0:1]
	s_andn2_b64 vcc, exec, s[4:5]
	s_cbranch_vccnz .LBB0_951
	s_waitcnt vmcnt(0)
	s_waitcnt vmcnt(0) lgkmcnt(0)
	s_barrier
	s_mov_b64 s[4:5], exec
	v_readlane_b32 s6, v255, 12
	v_readlane_b32 s7, v255, 13
	s_and_b64 s[6:7], s[4:5], s[6:7]
	s_mov_b64 exec, s[6:7]
	s_cbranch_execz .LBB0_950
	v_readlane_b32 s10, v255, 11
	v_readlane_b32 s14, v255, 9
	v_readlane_b32 s15, v255, 10
	v_mov_b32_e32 v4, 0x20160
	ds_read_b32 v4, v4
	s_lshl_b32 s10, s10, 8
	s_add_u32 s10, s14, s10
	s_addc_u32 s11, s15, 0
	v_mov_b32_e32 v5, 0x2000
	v_mov_b32_e32 v6, 1
	v_mov_b32_e32 v2, 0x3000
	s_mov_b32 s6, 0
	global_atomic_add v5, v6, s[10:11] offset:1024
	buffer_inv sc1
	global_load_dword v2, v2, s[14:15] offset:896 sc1
	s_waitcnt lgkmcnt(0)
.Lxl_spin_0:
	global_load_dword v6, v5, s[10:11] offset:1024 sc1
	s_waitcnt vmcnt(0)
	v_cmp_ne_u32_e32 vcc, 0, v2
	s_cbranch_vccnz .Lxl_full_0
	v_cmp_ge_u32_e32 vcc, v6, v4
	s_cbranch_vccnz .LBB0_950
	s_sleep 1
	s_add_u32 s6, s6, 1
	s_cmp_lt_u32 s6, 0x40000
	s_cbranch_scc1 .Lxl_spin_0
	s_branch .LBB0_950
.Lxl_full_0:
	s_add_i32 s6, 0, 0x20160
	v_mov_b32_e32 v2, s6
	s_waitcnt vmcnt(0) expcnt(0) lgkmcnt(0)
	ds_read_b32 v4, v2
	s_add_i32 s6, 0, 0x20164
	v_mov_b32_e32 v2, s6
	ds_read_b32 v2, v2
	s_waitcnt lgkmcnt(1)
	v_cmp_ne_u32_e32 vcc, 0, v4
	s_cbranch_vccnz .LBB0_916
	v_readlane_b32 s6, v255, 0
	v_readlane_b32 s7, v255, 1
	s_load_dwordx2 s[10:11], s[6:7], 0x4
	v_readlane_b32 s16, v255, 9
	v_readlane_b32 s17, v255, 10
	s_add_u32 s6, s16, 0x1000
	s_addc_u32 s7, s17, 0
	s_add_u32 s8, s16, 0x1100
	s_addc_u32 s9, s17, 0
	v_readlane_b32 s14, v255, 2
	s_waitcnt lgkmcnt(0)
	s_mul_i32 s10, s10, s14
	s_add_u32 s14, s16, 0x1200
	s_addc_u32 s15, s17, 0
	s_add_u32 s16, s16, 0x1300
	s_mul_i32 s10, s10, s11
	s_addc_u32 s17, s17, 0
	s_mov_b32 s11, 1
	v_mov_b32_e32 v18, 0
	s_branch .LBB0_904

.LBB0_979:
	s_and_b64 s[0:1], s[8:9], s[6:7]
	s_andn2_b64 vcc, exec, s[0:1]
	s_cbranch_vccnz .LBB0_1031
	s_waitcnt vmcnt(0)
	s_waitcnt lgkmcnt(0)
	s_barrier
	s_mov_b64 s[0:1], exec
	v_readlane_b32 s6, v255, 12
	v_readlane_b32 s7, v255, 13
	s_and_b64 s[6:7], s[0:1], s[6:7]
	s_mov_b64 exec, s[6:7]
	s_cbranch_execz .LBB0_1030
	v_readlane_b32 s10, v255, 11
	v_readlane_b32 s12, v255, 9
	v_readlane_b32 s13, v255, 10
	v_mov_b32_e32 v68, 0x20160
	ds_read_b32 v68, v68
	s_lshl_b32 s10, s10, 8
	s_add_u32 s10, s12, s10
	s_addc_u32 s11, s13, 0
	v_mov_b32_e32 v69, 0x2000
	v_mov_b32_e32 v70, 1
	v_mov_b32_e32 v66, 0x3000
	s_mov_b32 s6, 0
	global_atomic_add v69, v70, s[10:11] offset:1024
	buffer_inv sc1
	global_load_dword v66, v66, s[12:13] offset:896 sc1
	s_waitcnt lgkmcnt(0)
	v_mul_u32_u24_e32 v68, 2, v68
.Lxl_spin_1:
	global_load_dword v70, v69, s[10:11] offset:1024 sc1
	s_waitcnt vmcnt(0)
	v_cmp_ne_u32_e32 vcc, 0, v66
	s_cbranch_vccnz .Lxl_full_1
	v_cmp_ge_u32_e32 vcc, v70, v68
	s_cbranch_vccnz .LBB0_1030
	s_sleep 1
	s_add_u32 s6, s6, 1
	s_cmp_lt_u32 s6, 0x40000
	s_cbranch_scc1 .Lxl_spin_1
	s_branch .LBB0_1030
.Lxl_full_1:
	s_add_i32 s6, 0, 0x20160
	v_mov_b32_e32 v66, s6
	s_waitcnt vmcnt(0) expcnt(0) lgkmcnt(0)
	ds_read_b32 v68, v66
	s_add_i32 s6, 0, 0x20164
	v_mov_b32_e32 v66, s6
	ds_read_b32 v66, v66
	s_waitcnt lgkmcnt(1)
	v_cmp_ne_u32_e32 vcc, 0, v68
	s_cbranch_vccnz .LBB0_996
	v_readlane_b32 s6, v255, 0
	v_readlane_b32 s7, v255, 1
	s_load_dwordx2 s[10:11], s[6:7], 0x4
	v_readlane_b32 s14, v255, 9
	v_readlane_b32 s15, v255, 10
	s_add_u32 s6, s14, 0x1000
	s_addc_u32 s7, s15, 0
	s_add_u32 s8, s14, 0x1100
	s_addc_u32 s9, s15, 0
	v_readlane_b32 s12, v255, 2
	s_waitcnt lgkmcnt(0)
	s_mul_i32 s20, s10, s12
	s_add_u32 s10, s14, 0x1200
	s_mul_i32 s20, s20, s11
	s_addc_u32 s11, s15, 0
	s_add_u32 s12, s14, 0x1300
	s_addc_u32 s13, s15, 0
	s_mov_b32 s21, 1
	v_mov_b32_e32 v82, 0
	s_branch .LBB0_984
